# scan loader: K and Q tiles requested one chunk ahead; the 19 redundant expert-weight tile loads of chunks >=47 collapsed onto one cache line
# speedup vs baseline: 1.0124x; 1.0124x over previous
; __device__ __forceinline__ void p4_scan(const Args& a, const Frame& F) {
;     ...
;             auto conv_load = [&](int it) {
;                 const float* cW; int cN, cn;
;                 if (it < 32768) { const int e = it >> 10, sb = it & 1023; ck0 = (sb >> 6) * 64; cn = (sb & 63) * 32 + (lane & 31); cN = 2048; cW = a.in[IN_W1] + (size_t)e * 1024 * 2048; cD = (bf16*)(a.ws + WS_W1T);
;                     const int up = cn >= 1024, nn = cn & 1023; crow = e * 2048 + (nn >> 7) * 256 + up * 128 + (nn & 127); }
;                 else { const int it2 = it - 32768, e = it2 >> 9, sb = it2 & 511; ck0 = (sb >> 5) * 64; cn = (sb & 31) * 32 + (lane & 31); cN = 1024; cW = a.in[IN_W2] + (size_t)e * 1024 * 1024; cD = (bf16*)(a.ws + WS_W2T); crow = e * 1024 + cn; }
; #pragma unroll
;                 for (int i = 0; i < 32; ++i) cv[i] = cW[(size_t)(ck0 + (lane >> 5) + 2 * i) * cN + cn];
;             };
;     ...
;             conv_load(lw);
.LBB0_490:
	v_and_b32_e32 v82, 0x3c0, v9
	v_or_b32_e32 v14, v82, v158
	v_mov_b32_e32 v9, v145
	v_mul_u32_u24_e32 v12, s54, v14
	v_lshl_add_u64 v[8:9], v[8:9], 2, s[56:57]
	v_lshlrev_b32_e32 v12, 2, v12
	v_mov_b32_e32 v13, v145
	v_lshl_add_u64 v[12:13], v[8:9], 0, v[12:13]
	global_load_dword v148, v[12:13], off
	v_or_b32_e32 v12, 2, v14
	v_mul_u32_u24_e32 v12, s54, v12
	v_lshlrev_b32_e32 v12, 2, v12
	v_mov_b32_e32 v13, v145
	v_lshl_add_u64 v[12:13], v[8:9], 0, v[12:13]
	global_load_dword v141, v[12:13], off
	v_or_b32_e32 v12, 4, v14
	v_mul_u32_u24_e32 v12, s54, v12
	v_lshlrev_b32_e32 v12, 2, v12
	v_mov_b32_e32 v13, v145
	v_lshl_add_u64 v[12:13], v[8:9], 0, v[12:13]
	global_load_dword v149, v[12:13], off
	v_or_b32_e32 v12, 6, v14
	v_mul_u32_u24_e32 v12, s54, v12
	v_lshlrev_b32_e32 v12, 2, v12
	v_mov_b32_e32 v13, v145
	v_lshl_add_u64 v[12:13], v[8:9], 0, v[12:13]
	global_load_dword v137, v[12:13], off
	v_or_b32_e32 v12, 8, v14
	v_mul_u32_u24_e32 v12, s54, v12
	v_lshlrev_b32_e32 v12, 2, v12
	v_mov_b32_e32 v13, v145
	v_lshl_add_u64 v[12:13], v[8:9], 0, v[12:13]
	global_load_dword v142, v[12:13], off
	v_or_b32_e32 v12, 10, v14
	v_mul_u32_u24_e32 v12, s54, v12
	v_lshlrev_b32_e32 v12, 2, v12
	v_mov_b32_e32 v13, v145
	v_lshl_add_u64 v[12:13], v[8:9], 0, v[12:13]
	global_load_dword v81, v[12:13], off
	v_or_b32_e32 v12, 12, v14
	v_mul_u32_u24_e32 v12, s54, v12
	v_lshlrev_b32_e32 v12, 2, v12
	v_mov_b32_e32 v13, v145
	v_lshl_add_u64 v[12:13], v[8:9], 0, v[12:13]
	global_load_dword v138, v[12:13], off
	v_or_b32_e32 v12, 14, v14
	v_mul_u32_u24_e32 v12, s54, v12
	v_lshlrev_b32_e32 v12, 2, v12
	v_mov_b32_e32 v13, v145
	v_lshl_add_u64 v[12:13], v[8:9], 0, v[12:13]
	global_load_dword v151, v[12:13], off
	v_or_b32_e32 v12, 16, v14
	v_mul_u32_u24_e32 v12, s54, v12
	v_lshlrev_b32_e32 v12, 2, v12
	v_mov_b32_e32 v13, v145
	v_lshl_add_u64 v[12:13], v[8:9], 0, v[12:13]
	global_load_dword v152, v[12:13], off
	v_or_b32_e32 v12, 18, v14
	v_mul_u32_u24_e32 v12, s54, v12
	v_lshlrev_b32_e32 v12, 2, v12
	v_mov_b32_e32 v13, v145
	v_lshl_add_u64 v[12:13], v[8:9], 0, v[12:13]
	global_load_dword v143, v[12:13], off
	v_or_b32_e32 v12, 20, v14
	v_mul_u32_u24_e32 v12, s54, v12
	v_lshlrev_b32_e32 v12, 2, v12
	v_mov_b32_e32 v13, v145
	v_lshl_add_u64 v[12:13], v[8:9], 0, v[12:13]
	global_load_dword v150, v[12:13], off
	v_or_b32_e32 v12, 22, v14
	v_mul_u32_u24_e32 v12, s54, v12
	v_lshlrev_b32_e32 v12, 2, v12
	v_mov_b32_e32 v13, v145
	v_lshl_add_u64 v[12:13], v[8:9], 0, v[12:13]
	global_load_dword v139, v[12:13], off
	v_or_b32_e32 v12, 24, v14
	v_mul_u32_u24_e32 v12, s54, v12
	v_lshlrev_b32_e32 v12, 2, v12
	v_mov_b32_e32 v13, v145
	v_lshl_add_u64 v[12:13], v[8:9], 0, v[12:13]
	global_load_dword v147, v[12:13], off
	v_or_b32_e32 v12, 26, v14
	v_mul_u32_u24_e32 v12, s54, v12
	v_lshlrev_b32_e32 v12, 2, v12
	v_mov_b32_e32 v13, v145
	v_lshl_add_u64 v[12:13], v[8:9], 0, v[12:13]
	global_load_dword v83, v[12:13], off
	v_or_b32_e32 v12, 28, v14
	v_mul_u32_u24_e32 v12, s54, v12
	v_lshlrev_b32_e32 v12, 2, v12
	v_mov_b32_e32 v13, v145
	v_lshl_add_u64 v[12:13], v[8:9], 0, v[12:13]
	global_load_dword v140, v[12:13], off
	v_or_b32_e32 v12, 30, v14
	v_mul_u32_u24_e32 v12, s54, v12
	v_lshlrev_b32_e32 v12, 2, v12
	v_mov_b32_e32 v13, v145
	v_lshl_add_u64 v[12:13], v[8:9], 0, v[12:13]
	global_load_dword v153, v[12:13], off
	v_or_b32_e32 v12, 32, v14
	v_mul_u32_u24_e32 v12, s54, v12
	v_lshlrev_b32_e32 v12, 2, v12
	v_mov_b32_e32 v13, v145
	v_lshl_add_u64 v[12:13], v[8:9], 0, v[12:13]
	global_load_dword v183, v[12:13], off
	v_or_b32_e32 v12, 34, v14
	v_mul_u32_u24_e32 v12, s54, v12
	v_lshlrev_b32_e32 v12, 2, v12
	v_mov_b32_e32 v13, v145
	v_lshl_add_u64 v[12:13], v[8:9], 0, v[12:13]
	global_load_dword v179, v[12:13], off
	v_or_b32_e32 v12, 36, v14
	v_mul_u32_u24_e32 v12, s54, v12
	v_lshlrev_b32_e32 v12, 2, v12
	v_mov_b32_e32 v13, v145
	v_lshl_add_u64 v[12:13], v[8:9], 0, v[12:13]
	global_load_dword v184, v[12:13], off
	v_or_b32_e32 v12, 38, v14
	v_mul_u32_u24_e32 v12, s54, v12
	v_lshlrev_b32_e32 v12, 2, v12
	v_mov_b32_e32 v13, v145
	v_lshl_add_u64 v[12:13], v[8:9], 0, v[12:13]
	global_load_dword v175, v[12:13], off
	v_or_b32_e32 v12, 40, v14
	v_mul_u32_u24_e32 v12, s54, v12
	v_lshlrev_b32_e32 v12, 2, v12
	v_mov_b32_e32 v13, v145
	v_lshl_add_u64 v[12:13], v[8:9], 0, v[12:13]
	global_load_dword v180, v[12:13], off
	v_or_b32_e32 v12, 42, v14
	v_mul_u32_u24_e32 v12, s54, v12
	v_lshlrev_b32_e32 v12, 2, v12
	v_mov_b32_e32 v13, v145
	v_lshl_add_u64 v[12:13], v[8:9], 0, v[12:13]
	global_load_dword v173, v[12:13], off
	v_or_b32_e32 v12, 44, v14
	v_mul_u32_u24_e32 v12, s54, v12
	v_lshlrev_b32_e32 v12, 2, v12
	v_mov_b32_e32 v13, v145
	v_lshl_add_u64 v[12:13], v[8:9], 0, v[12:13]
	global_load_dword v176, v[12:13], off
	v_or_b32_e32 v12, 46, v14
	v_mul_u32_u24_e32 v12, s54, v12
	v_lshlrev_b32_e32 v12, 2, v12
	v_mov_b32_e32 v13, v145
	v_lshl_add_u64 v[12:13], v[8:9], 0, v[12:13]
	global_load_dword v186, v[12:13], off
	v_or_b32_e32 v12, 48, v14
	v_mul_u32_u24_e32 v12, s54, v12
	v_lshlrev_b32_e32 v12, 2, v12
	v_mov_b32_e32 v13, v145
	v_lshl_add_u64 v[12:13], v[8:9], 0, v[12:13]
	global_load_dword v187, v[12:13], off
	v_or_b32_e32 v12, 50, v14
	v_mul_u32_u24_e32 v12, s54, v12
	v_lshlrev_b32_e32 v12, 2, v12
	v_mov_b32_e32 v13, v145
	v_lshl_add_u64 v[12:13], v[8:9], 0, v[12:13]
	global_load_dword v181, v[12:13], off
	v_or_b32_e32 v12, 52, v14
; __device__ __forceinline__ void p4_scan(const Args& a, const Frame& F) {
;     ...
;             auto prefetch = [&](int ci) {
;                 const int base = chunk_base(ci);
; #pragma unroll
;                 for (int i = 0; i < 8; ++i) { const int p = ht + 256 * i, row = p >> 4, c16 = p & 15; const int tok = base + (dir ? 127 - row : row);
;                     pq[i] = *(const u32x4*)(QKC + (size_t)tok * 1024 + h * 128 + c16 * 8); pk[i] = *(const u32x4*)(QKC + (size_t)tok * 1024 + 512 + h * 128 + c16 * 8); }
;     ...
;             auto conv_load = [&](int it) {
;                 const float* cW; int cN, cn;
;                 if (it < 32768) { const int e = it >> 10, sb = it & 1023; ck0 = (sb >> 6) * 64; cn = (sb & 63) * 32 + (lane & 31); cN = 2048; cW = a.in[IN_W1] + (size_t)e * 1024 * 2048; cD = (bf16*)(a.ws + WS_W1T);
;                     const int up = cn >= 1024, nn = cn & 1023; crow = e * 2048 + (nn >> 7) * 256 + up * 128 + (nn & 127); }
;                 else { const int it2 = it - 32768, e = it2 >> 9, sb = it2 & 511; ck0 = (sb >> 5) * 64; cn = (sb & 31) * 32 + (lane & 31); cN = 1024; cW = a.in[IN_W2] + (size_t)e * 1024 * 1024; cD = (bf16*)(a.ws + WS_W2T); crow = e * 1024 + cn; }
; #pragma unroll
;                 for (int i = 0; i < 32; ++i) cv[i] = cW[(size_t)(ck0 + (lane >> 5) + 2 * i) * cN + cn];
;             };
	v_mul_u32_u24_e32 v12, s54, v12
	v_lshlrev_b32_e32 v12, 2, v12
	v_mov_b32_e32 v13, v145
	v_lshl_add_u64 v[12:13], v[8:9], 0, v[12:13]
	global_load_dword v185, v[12:13], off
	v_or_b32_e32 v12, 54, v14
	v_mul_u32_u24_e32 v12, s54, v12
	v_lshlrev_b32_e32 v12, 2, v12
	v_mov_b32_e32 v13, v145
	v_lshl_add_u64 v[12:13], v[8:9], 0, v[12:13]
	global_load_dword v177, v[12:13], off
	v_or_b32_e32 v12, 56, v14
	v_mul_u32_u24_e32 v12, s54, v12
	v_lshlrev_b32_e32 v12, 2, v12
	v_mov_b32_e32 v13, v145
	v_lshl_add_u64 v[12:13], v[8:9], 0, v[12:13]
	global_load_dword v182, v[12:13], off
	v_or_b32_e32 v12, 58, v14
	v_mul_u32_u24_e32 v12, s54, v12
	v_lshlrev_b32_e32 v12, 2, v12
	v_mov_b32_e32 v13, v145
	v_lshl_add_u64 v[12:13], v[8:9], 0, v[12:13]
	global_load_dword v174, v[12:13], off
	v_or_b32_e32 v12, 60, v14
	v_mul_u32_u24_e32 v12, s54, v12
	v_lshlrev_b32_e32 v12, 2, v12
	v_mov_b32_e32 v13, v145
	v_lshl_add_u64 v[12:13], v[8:9], 0, v[12:13]
	global_load_dword v178, v[12:13], off
	v_or_b32_e32 v12, 62, v14
	v_mul_u32_u24_e32 v12, s54, v12
	v_lshlrev_b32_e32 v12, 2, v12
	v_mov_b32_e32 v13, v145
	v_lshl_add_u64 v[8:9], v[8:9], 0, v[12:13]
	global_load_dword v188, v[8:9], off
	s_lshl_b32 s44, s44, 1
	s_add_u32 s54, s20, s44
	s_addc_u32 s55, s21, 0
	s_lshl_b32 s33, s33, 1
	s_add_u32 s54, s54, s33
	s_addc_u32 s55, s55, 0
	v_mov_b32_e32 v87, v145
	v_lshl_add_u64 v[86:87], s[54:55], 0, v[86:87]
	s_add_i32 s54, s34, s35
	v_mov_b64_e32 v[8:9], s[38:39]
	s_add_i32 s33, 0, 0x23430
	v_mad_i64_i32 v[88:89], s[34:35], v88, s95, v[8:9]
	v_mad_i64_i32 v[90:91], s[34:35], v90, s95, v[8:9]
	s_add_i32 s54, s54, 0x10000
	v_add_u32_e32 v12, s33, v11
	s_lshl_b32 s33, s58, 13
	s_xor_b32 s34, s54, 0x80
	s_add_u32 s54, s16, s44
	v_add_u32_e32 v11, s89, v11
	s_addc_u32 s55, s17, 0
	v_lshl_add_u64 v[92:93], s[54:55], 0, v[144:145]
	s_mov_b32 s44, 0
	v_mov_b32_e32 v136, 0
	v_add_u32_e32 v134, v12, v10
	v_add_u32_e32 v135, v11, v10
	v_add_u32_e32 v214, s34, v96
	v_ashrrev_i32_e32 v215, 31, v214
	v_lshlrev_b64 v[214:215], 11, v[214:215]
	v_lshl_add_u64 v[214:215], v[92:93], 0, v[214:215]
	global_load_dwordx4 v[220:223], v[214:215], off offset:1024
	v_add_u32_e32 v214, s34, v97
	v_ashrrev_i32_e32 v215, 31, v214
	v_lshlrev_b64 v[214:215], 11, v[214:215]
	v_lshl_add_u64 v[214:215], v[92:93], 0, v[214:215]
	global_load_dwordx4 v[224:227], v[214:215], off offset:1024
	v_add_u32_e32 v214, s34, v98
	v_ashrrev_i32_e32 v215, 31, v214
	v_lshlrev_b64 v[214:215], 11, v[214:215]
	v_lshl_add_u64 v[214:215], v[92:93], 0, v[214:215]
	global_load_dwordx4 v[228:231], v[214:215], off offset:1024
	v_add_u32_e32 v214, s34, v99
	v_ashrrev_i32_e32 v215, 31, v214
	v_lshlrev_b64 v[214:215], 11, v[214:215]
	v_lshl_add_u64 v[214:215], v[92:93], 0, v[214:215]
	global_load_dwordx4 v[232:235], v[214:215], off offset:1024
	v_add_u32_e32 v214, s34, v100
	v_ashrrev_i32_e32 v215, 31, v214
	v_lshlrev_b64 v[214:215], 11, v[214:215]
	v_lshl_add_u64 v[214:215], v[92:93], 0, v[214:215]
	global_load_dwordx4 v[236:239], v[214:215], off offset:1024
	v_add_u32_e32 v214, s34, v101
	v_ashrrev_i32_e32 v215, 31, v214
	v_lshlrev_b64 v[214:215], 11, v[214:215]
	v_lshl_add_u64 v[214:215], v[92:93], 0, v[214:215]
	global_load_dwordx4 v[240:243], v[214:215], off offset:1024
	v_add_u32_e32 v214, s34, v102
	v_ashrrev_i32_e32 v215, 31, v214
	v_lshlrev_b64 v[214:215], 11, v[214:215]
	v_lshl_add_u64 v[214:215], v[92:93], 0, v[214:215]
	global_load_dwordx4 v[244:247], v[214:215], off offset:1024
	v_add_u32_e32 v214, s34, v103
	v_ashrrev_i32_e32 v215, 31, v214
	v_lshlrev_b64 v[214:215], 11, v[214:215]
	v_lshl_add_u64 v[214:215], v[92:93], 0, v[214:215]
	global_load_dwordx4 v[248:251], v[214:215], off offset:1024
	v_add_u32_e32 v214, s34, v96
	v_ashrrev_i32_e32 v215, 31, v214
	v_lshlrev_b64 v[214:215], 11, v[214:215]
	v_lshl_add_u64 v[214:215], v[92:93], 0, v[214:215]
	global_load_dwordx4 v[16:19], v[214:215], off
	v_add_u32_e32 v214, s34, v97
	v_ashrrev_i32_e32 v215, 31, v214
	v_lshlrev_b64 v[214:215], 11, v[214:215]
	v_lshl_add_u64 v[214:215], v[92:93], 0, v[214:215]
	global_load_dwordx4 v[20:23], v[214:215], off
	v_add_u32_e32 v214, s34, v98
	v_ashrrev_i32_e32 v215, 31, v214
	v_lshlrev_b64 v[214:215], 11, v[214:215]
	v_lshl_add_u64 v[214:215], v[92:93], 0, v[214:215]
	global_load_dwordx4 v[24:27], v[214:215], off
	v_add_u32_e32 v214, s34, v99
	v_ashrrev_i32_e32 v215, 31, v214
	v_lshlrev_b64 v[214:215], 11, v[214:215]
	v_lshl_add_u64 v[214:215], v[92:93], 0, v[214:215]
	global_load_dwordx4 v[28:31], v[214:215], off
	v_add_u32_e32 v214, s34, v100
	v_ashrrev_i32_e32 v215, 31, v214
	v_lshlrev_b64 v[214:215], 11, v[214:215]
	v_lshl_add_u64 v[214:215], v[92:93], 0, v[214:215]
	global_load_dwordx4 v[32:35], v[214:215], off
	v_add_u32_e32 v214, s34, v101
	v_ashrrev_i32_e32 v215, 31, v214
	v_lshlrev_b64 v[214:215], 11, v[214:215]
	v_lshl_add_u64 v[214:215], v[92:93], 0, v[214:215]
	global_load_dwordx4 v[36:39], v[214:215], off
	v_add_u32_e32 v214, s34, v102
	v_ashrrev_i32_e32 v215, 31, v214
	v_lshlrev_b64 v[214:215], 11, v[214:215]
	v_lshl_add_u64 v[214:215], v[92:93], 0, v[214:215]
	global_load_dwordx4 v[40:43], v[214:215], off
	v_add_u32_e32 v214, s34, v103
	v_ashrrev_i32_e32 v215, 31, v214
	v_lshlrev_b64 v[214:215], 11, v[214:215]
	v_lshl_add_u64 v[214:215], v[92:93], 0, v[214:215]
	global_load_dwordx4 v[44:47], v[214:215], off
	s_branch .LBB0_492

; __device__ __forceinline__ void p4_scan(const Args& a, const Frame& F) {
;     ...
;             auto prefetch = [&](int ci) {
;                 const int base = chunk_base(ci);
; #pragma unroll
;                 for (int i = 0; i < 8; ++i) { const int p = ht + 256 * i, row = p >> 4, c16 = p & 15; const int tok = base + (dir ? 127 - row : row);
;                     pq[i] = *(const u32x4*)(QKC + (size_t)tok * 1024 + h * 128 + c16 * 8); pk[i] = *(const u32x4*)(QKC + (size_t)tok * 1024 + 512 + h * 128 + c16 * 8); }
; #pragma unroll
;                 for (int i = 0; i < 2; ++i) { const int p = ht + 256 * i, row = p >> 2, cc = p & 3; const int tok = base + (dir ? 127 - row : row);
;                     pv[i] = *(const u32x4*)(PV + (size_t)tok * 512 + h * 128 + vs * 32 + cc * 8); pga[i] = GS[(size_t)hd * TA + tok]; }
; #pragma unroll
;                 for (int i = 0; i < 2; ++i) { const int idx = ht + 256 * i; if (idx < 384) { const int row = idx & 127, arr = idx >> 7; const int tok = base + (dir ? 127 - row : row); pgl[i] = GS[(size_t)(arr * 8 + hd) * TA + tok]; } }
;                 pbt = CH[(hd * 528 + (base >> 7)) * 2]; ppx = CH[(hd * 528 + (base >> 7)) * 2 + 1];
;     ...
;             for (int ci = 0; ci < 66; ++ci) {
;                 const float M127 = fmaxf(pmx, mcar), mnew = btot + M127;
;                 const int cnx = ci + 1 < 66 ? ci + 1 : 65;
;                 prefetch(cnx);
.LBB0_492:
	s_waitcnt vmcnt(8)
	s_add_i32 s35, s44, 1
	s_cmpk_eq_i32 s44, 0x41
	s_cselect_b32 s56, s44, s35
	s_sub_i32 s58, 0x41, s56
	v_sub_co_u32_e64 v8, s[54:55], s56, 2
	s_and_b64 s[56:57], s[4:5], exec
	v_readfirstlane_b32 s56, v8
	s_cselect_b32 s56, s56, s58
	s_lshl_b32 s56, s56, 7
	s_add_i32 s56, s56, s33
	s_and_b64 s[54:55], s[54:55], exec
	s_cselect_b32 s56, s34, s56
	v_add_u32_e32 v8, s56, v104
	v_ashrrev_i32_e32 v9, 31, v8
	v_lshlrev_b64 v[10:11], 10, v[8:9]
	v_lshl_add_u64 v[10:11], v[86:87], 0, v[10:11]
	v_lshl_add_u64 v[8:9], v[8:9], 2, s[50:51]
	global_load_dwordx4 v[12:15], v[10:11], off
	global_load_dword v172, v[8:9], off
	v_add_u32_e32 v8, s56, v105
	v_ashrrev_i32_e32 v9, 31, v8
	v_lshlrev_b64 v[10:11], 10, v[8:9]
	v_lshl_add_u64 v[10:11], v[86:87], 0, v[10:11]
	v_lshl_add_u64 v[94:95], v[8:9], 2, s[50:51]
	global_load_dwordx4 v[8:11], v[10:11], off
	s_nop 0
	global_load_dword v171, v[94:95], off
	v_or_b32_e32 v94, s56, v106
	v_ashrrev_i32_e32 v95, 31, v94
	s_and_saveexec_b64 s[54:55], s[6:7]
	s_cbranch_execz .LBB0_494
	v_lshl_add_u64 v[190:191], v[94:95], 2, v[88:89]
	global_load_dword v108, v[190:191], off

; #define LDS_BARRIER() do { asm volatile("s_waitcnt lgkmcnt(0)" ::: "memory"); __builtin_amdgcn_s_barrier(); asm volatile("" ::: "memory"); } while (0)
; __device__ __forceinline__ void p4_scan(const Args& a, const Frame& F) {
;     ...
;             auto conv_load = [&](int it) {
;                 const float* cW; int cN, cn;
;                 if (it < 32768) { const int e = it >> 10, sb = it & 1023; ck0 = (sb >> 6) * 64; cn = (sb & 63) * 32 + (lane & 31); cN = 2048; cW = a.in[IN_W1] + (size_t)e * 1024 * 2048; cD = (bf16*)(a.ws + WS_W1T);
;                     const int up = cn >= 1024, nn = cn & 1023; crow = e * 2048 + (nn >> 7) * 256 + up * 128 + (nn & 127); }
;                 else { const int it2 = it - 32768, e = it2 >> 9, sb = it2 & 511; ck0 = (sb >> 5) * 64; cn = (sb & 31) * 32 + (lane & 31); cN = 1024; cW = a.in[IN_W2] + (size_t)e * 1024 * 1024; cD = (bf16*)(a.ws + WS_W2T); crow = e * 1024 + cn; }
; #pragma unroll
;                 for (int i = 0; i < 32; ++i) cv[i] = cW[(size_t)(ck0 + (lane >> 5) + 2 * i) * cN + cn];
;             };
;     ...
;                 const float M127 = fmaxf(pmx, mcar), mnew = btot + M127;
;                 const int cnx = ci + 1 < 66 ? ci + 1 : 65;
;                 prefetch(cnx);
;                 commitK((ci & 1) ? S_K0 : S_K1);
;                 if (ci < 48) conv_store();
;                 conv_load(lw + 1024 * ((ci + 1) % 48));
;                 LDS_BARRIER();
.LBB0_502:
	s_cmp_ge_u32 s35, 48
	s_cselect_b32 s56, 0, s56
	v_and_b32_e32 v82, 0x3c0, v48
	v_max_f32_e32 v49, v136, v136
	v_max_f32_e32 v50, v85, v85
	v_or_b32_e32 v52, v82, v158
	v_max_f32_e32 v49, v50, v49
	v_mul_u32_u24_e32 v50, s56, v52
	v_add_f32_e32 v136, v84, v49
	v_lshl_add_u64 v[48:49], v[144:145], 2, s[58:59]
	v_lshlrev_b32_e32 v144, 2, v50
	v_lshl_add_u64 v[50:51], v[48:49], 0, v[144:145]
	global_load_dword v148, v[50:51], off
	v_or_b32_e32 v50, 2, v52
	v_mul_u32_u24_e32 v50, s56, v50
	v_lshlrev_b32_e32 v144, 2, v50
	v_lshl_add_u64 v[50:51], v[48:49], 0, v[144:145]
	global_load_dword v141, v[50:51], off
	v_or_b32_e32 v50, 4, v52
	v_mul_u32_u24_e32 v50, s56, v50
	v_lshlrev_b32_e32 v144, 2, v50
	v_lshl_add_u64 v[50:51], v[48:49], 0, v[144:145]
	global_load_dword v149, v[50:51], off
	v_or_b32_e32 v50, 6, v52
	v_mul_u32_u24_e32 v50, s56, v50
	v_lshlrev_b32_e32 v144, 2, v50
	v_lshl_add_u64 v[50:51], v[48:49], 0, v[144:145]
	global_load_dword v137, v[50:51], off
	v_or_b32_e32 v50, 8, v52
	v_mul_u32_u24_e32 v50, s56, v50
	v_lshlrev_b32_e32 v144, 2, v50
	v_lshl_add_u64 v[50:51], v[48:49], 0, v[144:145]
	global_load_dword v142, v[50:51], off
	v_or_b32_e32 v50, 10, v52
	v_mul_u32_u24_e32 v50, s56, v50
	v_lshlrev_b32_e32 v144, 2, v50
	v_lshl_add_u64 v[50:51], v[48:49], 0, v[144:145]
	global_load_dword v81, v[50:51], off
	v_or_b32_e32 v50, 12, v52
	v_mul_u32_u24_e32 v50, s56, v50
	v_lshlrev_b32_e32 v144, 2, v50
	v_lshl_add_u64 v[50:51], v[48:49], 0, v[144:145]
	global_load_dword v138, v[50:51], off
	v_or_b32_e32 v50, 14, v52
	v_mul_u32_u24_e32 v50, s56, v50
	v_lshlrev_b32_e32 v144, 2, v50
	v_lshl_add_u64 v[50:51], v[48:49], 0, v[144:145]
	global_load_dword v151, v[50:51], off
	v_or_b32_e32 v50, 16, v52
	v_mul_u32_u24_e32 v50, s56, v50
	v_lshlrev_b32_e32 v144, 2, v50
	v_lshl_add_u64 v[50:51], v[48:49], 0, v[144:145]
	global_load_dword v152, v[50:51], off
	v_or_b32_e32 v50, 18, v52
	v_mul_u32_u24_e32 v50, s56, v50
	v_lshlrev_b32_e32 v144, 2, v50
	v_lshl_add_u64 v[50:51], v[48:49], 0, v[144:145]
	global_load_dword v143, v[50:51], off
	v_or_b32_e32 v50, 20, v52
	v_mul_u32_u24_e32 v50, s56, v50
	v_lshlrev_b32_e32 v144, 2, v50
	v_lshl_add_u64 v[50:51], v[48:49], 0, v[144:145]
	global_load_dword v150, v[50:51], off
	v_or_b32_e32 v50, 22, v52
	v_mul_u32_u24_e32 v50, s56, v50
	v_lshlrev_b32_e32 v144, 2, v50
	v_lshl_add_u64 v[50:51], v[48:49], 0, v[144:145]
	global_load_dword v139, v[50:51], off
	v_or_b32_e32 v50, 24, v52
	v_mul_u32_u24_e32 v50, s56, v50
	v_lshlrev_b32_e32 v144, 2, v50
	v_lshl_add_u64 v[50:51], v[48:49], 0, v[144:145]
	global_load_dword v147, v[50:51], off
	v_or_b32_e32 v50, 26, v52
	v_mul_u32_u24_e32 v50, s56, v50
	v_lshlrev_b32_e32 v144, 2, v50
	v_lshl_add_u64 v[50:51], v[48:49], 0, v[144:145]
	global_load_dword v83, v[50:51], off
	v_or_b32_e32 v50, 28, v52
	v_mul_u32_u24_e32 v50, s56, v50
	v_lshlrev_b32_e32 v144, 2, v50
	v_lshl_add_u64 v[50:51], v[48:49], 0, v[144:145]
	global_load_dword v140, v[50:51], off
	v_or_b32_e32 v50, 30, v52
	v_mul_u32_u24_e32 v50, s56, v50
	v_lshlrev_b32_e32 v144, 2, v50
	v_lshl_add_u64 v[50:51], v[48:49], 0, v[144:145]
	global_load_dword v153, v[50:51], off
	v_or_b32_e32 v50, 32, v52
	v_mul_u32_u24_e32 v50, s56, v50
	v_lshlrev_b32_e32 v144, 2, v50
	v_lshl_add_u64 v[50:51], v[48:49], 0, v[144:145]
	global_load_dword v183, v[50:51], off
	v_or_b32_e32 v50, 34, v52
	v_mul_u32_u24_e32 v50, s56, v50
	v_lshlrev_b32_e32 v144, 2, v50
	v_lshl_add_u64 v[50:51], v[48:49], 0, v[144:145]
	global_load_dword v179, v[50:51], off
	v_or_b32_e32 v50, 36, v52
	v_mul_u32_u24_e32 v50, s56, v50
	v_lshlrev_b32_e32 v144, 2, v50
	v_lshl_add_u64 v[50:51], v[48:49], 0, v[144:145]
	global_load_dword v184, v[50:51], off
	v_or_b32_e32 v50, 38, v52
	v_mul_u32_u24_e32 v50, s56, v50
	v_lshlrev_b32_e32 v144, 2, v50
	v_lshl_add_u64 v[50:51], v[48:49], 0, v[144:145]
	global_load_dword v175, v[50:51], off
	v_or_b32_e32 v50, 40, v52
	v_mul_u32_u24_e32 v50, s56, v50
	v_lshlrev_b32_e32 v144, 2, v50
	v_lshl_add_u64 v[50:51], v[48:49], 0, v[144:145]
	global_load_dword v180, v[50:51], off
	v_or_b32_e32 v50, 42, v52
	v_mul_u32_u24_e32 v50, s56, v50
	v_lshlrev_b32_e32 v144, 2, v50
	v_lshl_add_u64 v[50:51], v[48:49], 0, v[144:145]
	global_load_dword v173, v[50:51], off
	v_or_b32_e32 v50, 44, v52
	v_mul_u32_u24_e32 v50, s56, v50
	v_lshlrev_b32_e32 v144, 2, v50
	v_lshl_add_u64 v[50:51], v[48:49], 0, v[144:145]
	global_load_dword v176, v[50:51], off
	v_or_b32_e32 v50, 46, v52
	v_mul_u32_u24_e32 v50, s56, v50
	v_lshlrev_b32_e32 v144, 2, v50
	v_lshl_add_u64 v[50:51], v[48:49], 0, v[144:145]
	global_load_dword v186, v[50:51], off
	v_or_b32_e32 v50, 48, v52
	v_mul_u32_u24_e32 v50, s56, v50
	v_lshlrev_b32_e32 v144, 2, v50
	v_lshl_add_u64 v[50:51], v[48:49], 0, v[144:145]
	global_load_dword v187, v[50:51], off
	v_or_b32_e32 v50, 50, v52
	v_mul_u32_u24_e32 v50, s56, v50
	v_lshlrev_b32_e32 v144, 2, v50
	v_lshl_add_u64 v[50:51], v[48:49], 0, v[144:145]
	global_load_dword v181, v[50:51], off
	v_or_b32_e32 v50, 52, v52
	v_mul_u32_u24_e32 v50, s56, v50
	v_lshlrev_b32_e32 v144, 2, v50
	v_lshl_add_u64 v[50:51], v[48:49], 0, v[144:145]
	global_load_dword v185, v[50:51], off
	v_or_b32_e32 v50, 54, v52
	v_mul_u32_u24_e32 v50, s56, v50
	v_lshlrev_b32_e32 v144, 2, v50
	v_lshl_add_u64 v[50:51], v[48:49], 0, v[144:145]
	global_load_dword v177, v[50:51], off
	v_or_b32_e32 v50, 56, v52
	v_mul_u32_u24_e32 v50, s56, v50
	v_lshlrev_b32_e32 v144, 2, v50
	v_lshl_add_u64 v[50:51], v[48:49], 0, v[144:145]
	global_load_dword v182, v[50:51], off
	v_or_b32_e32 v50, 58, v52
	v_mul_u32_u24_e32 v50, s56, v50
	v_lshlrev_b32_e32 v144, 2, v50
	v_lshl_add_u64 v[50:51], v[48:49], 0, v[144:145]
	global_load_dword v174, v[50:51], off
	v_or_b32_e32 v50, 60, v52
	v_mul_u32_u24_e32 v50, s56, v50
	v_lshlrev_b32_e32 v144, 2, v50
	v_lshl_add_u64 v[50:51], v[48:49], 0, v[144:145]
	global_load_dword v178, v[50:51], off
	v_or_b32_e32 v50, 62, v52
	v_mul_u32_u24_e32 v50, s56, v50
	v_lshlrev_b32_e32 v144, 2, v50
	v_lshl_add_u64 v[48:49], v[48:49], 0, v[144:145]
	global_load_dword v188, v[48:49], off
	s_waitcnt lgkmcnt(0)
	s_barrier
; #define LAS __attribute__((address_space(3)))
; __device__ __forceinline__ unsigned f2bf(float f) { unsigned u = __builtin_bit_cast(unsigned, f); return (u + 0x7fffu + ((u >> 16) & 1u)) >> 16; }
; __device__ __forceinline__ float bflo(unsigned w) { return __uint_as_float(w << 16); }
; __device__ __forceinline__ float bfhi(unsigned w) { return __uint_as_float(w & 0xffff0000u); }
; __device__ __forceinline__ void p4_scan(const Args& a, const Frame& F) {
;     ...
;             auto prefetch = [&](int ci) {
;                 const int base = chunk_base(ci);
; #pragma unroll
;                 for (int i = 0; i < 8; ++i) { const int p = ht + 256 * i, row = p >> 4, c16 = p & 15; const int tok = base + (dir ? 127 - row : row);
;                     pq[i] = *(const u32x4*)(QKC + (size_t)tok * 1024 + h * 128 + c16 * 8); pk[i] = *(const u32x4*)(QKC + (size_t)tok * 1024 + 512 + h * 128 + c16 * 8); }
;     ...
;             auto commitQ = [&]() {
; #pragma unroll
;                 for (int i = 0; i < 8; ++i) { const int p = ht + 256 * i, row = p >> 4, c16 = p & 15; *(LAS u32x4*)(L + S_QS + row * SP + c16 * 16) = pq[i]; } };
;             auto commitV = [&](float mprev, int vabuf) {
; #pragma unroll
;                 for (int i = 0; i < 2; ++i) { const int p = ht + 256 * i, row = p >> 2, cc = p & 3; const unsigned wv[4] = {pv[i].x, pv[i].y, pv[i].z, pv[i].w};
;                     const float av = __expf(pga[i] - fmaxf(ppx, mprev));
; #pragma unroll
;                     for (int j = 0; j < 4; ++j) { const unsigned sc2 = pg8::cvt_pk_bf16(av * bflo(wv[j]), av * bfhi(wv[j]));
;                         *(LAS bf16*)(L + S_VT + (cc * 8 + 2 * j) * SP + row * 2) = (bf16)(wv[j] & 0xffffu); *(LAS bf16*)(L + S_VT + (cc * 8 + 2 * j + 1) * SP + row * 2) = (bf16)(wv[j] >> 16);
;                         *(LAS bf16*)(L + vabuf + (cc * 8 + 2 * j) * SP + row * 2) = (bf16)(sc2 & 0xffffu); *(LAS bf16*)(L + vabuf + (cc * 8 + 2 * j + 1) * SP + row * 2) = (bf16)(sc2 >> 16); }
;                     if (cc == 0) *(LAS bf16*)(L + vabuf + 32 * SP + row * 2) = (bf16)f2bf(av); }
; #pragma unroll
;                 for (int i = 0; i < 2; ++i) { const int idx = ht + 256 * i; if (idx < 384) { const int row = idx & 127, arr = idx >> 7; *(LAS float*)(L + S_GL + arr * 512 + row * 4) = pgl[i]; } }
;             };
	s_waitcnt vmcnt(40)
	ds_write_b128 v119, v[16:19]
	ds_write_b128 v120, v[20:23]
	ds_write_b128 v121, v[24:27]
	ds_write_b128 v122, v[28:31]
	ds_write_b128 v123, v[32:35]
	ds_write_b128 v124, v[36:39]
	ds_write_b128 v125, v[40:43]
	ds_write_b128 v126, v[44:47]
	v_add_u32_e32 v214, s98, v96
	v_ashrrev_i32_e32 v215, 31, v214
	v_lshlrev_b64 v[214:215], 11, v[214:215]
	v_lshl_add_u64 v[214:215], v[92:93], 0, v[214:215]
	global_load_dwordx4 v[16:19], v[214:215], off
	v_add_u32_e32 v214, s98, v97
	v_ashrrev_i32_e32 v215, 31, v214
	v_lshlrev_b64 v[214:215], 11, v[214:215]
	v_lshl_add_u64 v[214:215], v[92:93], 0, v[214:215]
	global_load_dwordx4 v[20:23], v[214:215], off
	v_add_u32_e32 v214, s98, v98
	v_ashrrev_i32_e32 v215, 31, v214
	v_lshlrev_b64 v[214:215], 11, v[214:215]
	v_lshl_add_u64 v[214:215], v[92:93], 0, v[214:215]
	global_load_dwordx4 v[24:27], v[214:215], off
	v_add_u32_e32 v214, s98, v99
	v_ashrrev_i32_e32 v215, 31, v214
	v_lshlrev_b64 v[214:215], 11, v[214:215]
	v_lshl_add_u64 v[214:215], v[92:93], 0, v[214:215]
	global_load_dwordx4 v[28:31], v[214:215], off
	v_add_u32_e32 v214, s98, v100
	v_ashrrev_i32_e32 v215, 31, v214
	v_lshlrev_b64 v[214:215], 11, v[214:215]
	v_lshl_add_u64 v[214:215], v[92:93], 0, v[214:215]
	global_load_dwordx4 v[32:35], v[214:215], off
	v_add_u32_e32 v214, s98, v101
	v_ashrrev_i32_e32 v215, 31, v214
	v_lshlrev_b64 v[214:215], 11, v[214:215]
	v_lshl_add_u64 v[214:215], v[92:93], 0, v[214:215]
	global_load_dwordx4 v[36:39], v[214:215], off
	v_add_u32_e32 v214, s98, v102
	v_ashrrev_i32_e32 v215, 31, v214
	v_lshlrev_b64 v[214:215], 11, v[214:215]
	v_lshl_add_u64 v[214:215], v[92:93], 0, v[214:215]
	global_load_dwordx4 v[40:43], v[214:215], off
	v_add_u32_e32 v214, s98, v103
	v_ashrrev_i32_e32 v215, 31, v214
	v_lshlrev_b64 v[214:215], 11, v[214:215]
	v_lshl_add_u64 v[214:215], v[92:93], 0, v[214:215]
	global_load_dwordx4 v[44:47], v[214:215], off
	v_max_f32_e32 v192, v95, v95
	v_max_f32_e32 v192, v192, v136
	v_sub_f32_e32 v193, v172, v192
	v_mul_f32_e32 v193, 0x3fb8aa3b, v193
	v_exp_f32_e32 v193, v193
	s_and_b64 s[54:55], s[54:55], exec
	v_lshlrev_b32_e32 v194, 16, v12
	v_and_b32_e32 v195, 0xffff0000, v12
	s_cselect_b32 s44, 0x1de20, s92
	v_mul_f32_e32 v194, v193, v194
	v_mul_f32_e32 v195, v193, v195
	v_cvt_pk_bf16_f32 v194, v194, v195
	v_add_u32_e32 v195, v128, v129
	s_add_i32 s44, s44, 0
	ds_write_b16 v127, v12
	ds_write_b16_d16_hi v195, v12 offset:272
	v_add_u32_e32 v12, s44, v129
	v_add_u32_e32 v196, v12, v118
	ds_write_b16 v196, v194
	ds_write_b16_d16_hi v196, v194 offset:272
	v_lshlrev_b32_e32 v194, 16, v13
	v_mul_f32_e32 v194, v193, v194
	v_and_b32_e32 v197, 0xffff0000, v13
	v_mul_f32_e32 v197, v193, v197
	v_cvt_pk_bf16_f32 v194, v194, v197
	ds_write_b16 v195, v13 offset:544
	ds_write_b16_d16_hi v195, v13 offset:816
	ds_write_b16 v196, v194 offset:544
	ds_write_b16_d16_hi v196, v194 offset:816
	v_lshlrev_b32_e32 v13, 16, v14
	v_mul_f32_e32 v13, v193, v13
	v_and_b32_e32 v194, 0xffff0000, v14
	v_mul_f32_e32 v194, v193, v194
	v_cvt_pk_bf16_f32 v13, v13, v194
	ds_write_b16 v195, v14 offset:1088
	ds_write_b16_d16_hi v195, v14 offset:1360
	ds_write_b16 v196, v13 offset:1088
	ds_write_b16_d16_hi v196, v13 offset:1360
	v_lshlrev_b32_e32 v13, 16, v15
	v_mul_f32_e32 v13, v193, v13
	v_and_b32_e32 v14, 0xffff0000, v15
	v_mul_f32_e32 v14, v193, v14
	v_cvt_pk_bf16_f32 v13, v13, v14
	ds_write_b16 v195, v15 offset:1632
	ds_write_b16_d16_hi v195, v15 offset:1904
	ds_write_b16 v196, v13 offset:1632
	ds_write_b16_d16_hi v196, v13 offset:1904
	s_and_saveexec_b64 s[54:55], s[10:11]
	v_bfe_u32 v13, v193, 16, 1
	v_add3_u32 v13, v193, v13, s93
	v_add_u32_e32 v14, s44, v118
	ds_write_b16_d16_hi v14, v13 offset:8704
	s_or_b64 exec, exec, s[54:55]
	v_sub_f32_e32 v13, v171, v192
	v_mul_f32_e32 v13, 0x3fb8aa3b, v13
	v_exp_f32_e32 v13, v13
	v_lshlrev_b32_e32 v14, 16, v8
	v_and_b32_e32 v15, 0xffff0000, v8
	v_mul_f32_e32 v14, v13, v14
	v_mul_f32_e32 v15, v13, v15
	v_cvt_pk_bf16_f32 v14, v14, v15
	ds_write_b16 v131, v8
	ds_write_b16_d16_hi v132, v8 offset:272
	v_add_u32_e32 v8, v12, v130
	v_lshlrev_b32_e32 v12, 16, v9
	ds_write_b16 v8, v14
	ds_write_b16_d16_hi v8, v14 offset:272
	v_mul_f32_e32 v12, v13, v12
	v_and_b32_e32 v14, 0xffff0000, v9
	v_mul_f32_e32 v14, v13, v14
	v_cvt_pk_bf16_f32 v12, v12, v14
	ds_write_b16 v132, v9 offset:544
	ds_write_b16_d16_hi v132, v9 offset:816
	ds_write_b16 v8, v12 offset:544
	ds_write_b16_d16_hi v8, v12 offset:816
	v_lshlrev_b32_e32 v9, 16, v10
	v_mul_f32_e32 v9, v13, v9
	v_and_b32_e32 v12, 0xffff0000, v10
	v_mul_f32_e32 v12, v13, v12
	v_cvt_pk_bf16_f32 v9, v9, v12
	ds_write_b16 v132, v10 offset:1088
	ds_write_b16_d16_hi v132, v10 offset:1360
	ds_write_b16 v8, v9 offset:1088
	ds_write_b16_d16_hi v8, v9 offset:1360
	v_lshlrev_b32_e32 v9, 16, v11
	v_mul_f32_e32 v9, v13, v9
	v_and_b32_e32 v10, 0xffff0000, v11
	v_mul_f32_e32 v10, v13, v10
	v_cvt_pk_bf16_f32 v9, v9, v10
	ds_write_b16 v132, v11 offset:1632
	ds_write_b16_d16_hi v132, v11 offset:1904
	ds_write_b16 v8, v9 offset:1632
	ds_write_b16_d16_hi v8, v9 offset:1904
	s_and_saveexec_b64 s[54:55], s[10:11]
	s_cbranch_execnz .LBB0_507
	s_or_b64 exec, exec, s[54:55]
	s_and_saveexec_b64 s[54:55], s[6:7]
	s_cbranch_execnz .LBB0_508
